# qkv epilogue: 144 v_pk_fma_f32 replaced by pairs of scalar f32 FMAs (packed f32 VALU issues slowly beside other waves' MFMAs)
# speedup vs baseline: 1.0232x; 1.0000x over previous
.LBB1_60:
	s_or_b64 exec, exec, s[0:1]
	v_lshl_add_u32 v0, v92, 2, v101
	s_barrier
	ds_write2_b32 v0, v18, v26 offset1:16
	ds_write2_b32 v0, v19, v27 offset0:68 offset1:84
	ds_write2_b32 v0, v20, v28 offset0:136 offset1:152
	ds_write2_b32 v0, v21, v29 offset0:204 offset1:220
	ds_write2_b32 v0, v22, v30 offset0:32 offset1:48
	ds_write2_b32 v0, v23, v31 offset0:100 offset1:116
	ds_write2_b32 v0, v24, v32 offset0:168 offset1:184
	ds_write2_b32 v0, v25, v33 offset0:236 offset1:252
	v_add_u32_e32 v1, 0x1000, v0
	v_add_u32_e32 v0, 0x1400, v0
	ds_write2_b32 v1, v2, v10 offset0:64 offset1:80
	ds_write2_b32 v1, v3, v11 offset0:132 offset1:148
	ds_write2_b32 v1, v4, v12 offset0:200 offset1:216
	ds_write2_b32 v0, v5, v13 offset0:12 offset1:28
	ds_write2_b32 v1, v6, v14 offset0:96 offset1:112
	ds_write2_b32 v1, v7, v15 offset0:164 offset1:180
	ds_write2_b32 v1, v8, v16 offset0:232 offset1:248
	ds_write2_b32 v0, v9, v17 offset0:44 offset1:60
	s_waitcnt lgkmcnt(0)
	s_barrier
	s_and_saveexec_b64 s[0:1], s[4:5]
	s_cbranch_execz .LBB1_62
	v_max3_f32 v0, v55, v54, v53
	v_max3_f32 v0, v0, v52, v51
	v_max3_f32 v0, v0, v50, v49
	v_max3_f32 v0, v0, v35, v48
	v_sub_f32_e32 v1, v55, v0
	v_mul_f32_e32 v1, 0x3fb8aa3b, v1
	v_sub_f32_e32 v2, v54, v0
	v_exp_f32_e32 v1, v1
	v_sub_f32_e32 v3, v53, v0
	v_mul_f32_e32 v2, 0x3fb8aa3b, v2
	v_exp_f32_e32 v2, v2
	v_mul_f32_e32 v3, 0x3fb8aa3b, v3
	v_sub_f32_e32 v5, v52, v0
	v_exp_f32_e32 v3, v3
	v_mul_f32_e32 v5, 0x3fb8aa3b, v5
	v_sub_f32_e32 v6, v51, v0
	v_exp_f32_e32 v5, v5
	v_mul_f32_e32 v6, 0x3fb8aa3b, v6
	v_sub_f32_e32 v7, v50, v0
	v_add_f32_e32 v4, 0, v1
	v_exp_f32_e32 v9, v6
	v_mul_f32_e32 v6, 0x3fb8aa3b, v7
	v_sub_f32_e32 v7, v49, v0
	v_add_f32_e32 v4, v4, v2
	v_exp_f32_e32 v11, v6
	v_mul_f32_e32 v6, 0x3fb8aa3b, v7
	v_sub_f32_e32 v7, v35, v0
	v_add_f32_e32 v4, v4, v3
	v_exp_f32_e32 v13, v6
	v_mul_f32_e32 v6, 0x3fb8aa3b, v7
	v_sub_f32_e32 v0, v48, v0
	v_add_f32_e32 v4, v4, v5
	v_exp_f32_e32 v7, v6
	v_mul_f32_e32 v0, 0x3fb8aa3b, v0
	v_add_f32_e32 v4, v4, v9
	v_exp_f32_e32 v0, v0
	v_add_f32_e32 v4, v4, v11
	v_add_f32_e32 v4, v4, v13
	v_add_f32_e32 v4, v4, v7
	v_add_f32_e32 v4, v4, v0
	v_rcp_f32_e32 v15, v4
	v_ashrrev_i32_e32 v35, 31, v34
	s_movk_i32 s0, 0xc5
	v_mul_f32_e32 v4, v15, v1
	v_mul_f32_e32 v20, v15, v0
	v_mad_u64_u32 v[0:1], s[0:1], v56, s0, v[34:35]
	s_movk_i32 s0, 0x110
	v_mul_f32_e32 v6, v15, v2
	v_mul_lo_u32 v2, v46, s0
	v_lshlrev_b64 v[0:1], 7, v[0:1]
	v_mul_f32_e32 v8, v15, v3
	v_mul_f32_e32 v10, v15, v5
	v_lshl_add_u32 v5, v47, 7, v2
	v_lshl_add_u64 v[0:1], s[6:7], 0, v[0:1]
	v_lshlrev_b32_e32 v2, 6, v47
	v_mov_b32_e32 v3, 0
	v_lshl_add_u64 v[22:23], v[0:1], 0, v[2:3]
	ds_read_b128 v[24:27], v5
	ds_read_b128 v[28:31], v5 offset:16
	ds_read_b128 v[32:35], v5 offset:3808
	ds_read_b128 v[36:39], v5 offset:32
	ds_read_b128 v[0:3], v5 offset:48
	ds_read_b128 v[40:43], v5 offset:7616
	ds_read_b128 v[44:47], v5 offset:3824
	ds_read_b128 v[48:51], v5 offset:11424
	ds_read_b128 v[52:55], v5 offset:7632
	s_waitcnt lgkmcnt(8)
	v_mul_f32_e32 v24, v4, v24
	v_mul_f32_e32 v25, v4, v25
	s_waitcnt lgkmcnt(6)
	v_fma_f32 v24, v6, v32, v24
	v_fma_f32 v25, v6, v33, v25
	ds_read_b128 v[56:59], v5 offset:15232
	ds_read_b128 v[60:63], v5 offset:19040
	ds_read_b128 v[64:67], v5 offset:11440
	s_waitcnt lgkmcnt(6)
	v_fma_f32 v24, v8, v40, v24
	v_fma_f32 v25, v8, v41, v25
	v_mul_f32_e32 v12, v15, v9
	s_waitcnt lgkmcnt(4)
	v_fma_f32 v24, v10, v48, v24
	v_fma_f32 v25, v10, v49, v25
	v_mul_f32_e32 v14, v15, v11
	s_waitcnt lgkmcnt(2)
	v_fma_f32 v24, v12, v56, v24
	v_fma_f32 v25, v12, v57, v25
	s_waitcnt lgkmcnt(1)
	v_fma_f32 v76, v14, v60, v24
	v_fma_f32 v77, v14, v61, v25
	v_mul_f32_e32 v24, v4, v26
	v_mul_f32_e32 v25, v4, v27
	v_fma_f32 v24, v6, v34, v24
	v_fma_f32 v25, v6, v35, v25
	v_fma_f32 v24, v8, v42, v24
	v_fma_f32 v25, v8, v43, v25
	v_fma_f32 v24, v10, v50, v24
	v_fma_f32 v25, v10, v51, v25
	ds_read_b128 v[68:71], v5 offset:15248
	ds_read_b128 v[72:75], v5 offset:19056
	v_fma_f32 v24, v12, v58, v24
	v_fma_f32 v25, v12, v59, v25
	v_fma_f32 v78, v14, v62, v24
	v_fma_f32 v79, v14, v63, v25
	v_mul_f32_e32 v24, v4, v28
	v_mul_f32_e32 v25, v4, v29
	v_fma_f32 v24, v6, v44, v24
	v_fma_f32 v25, v6, v45, v25
	v_fma_f32 v24, v8, v52, v24
	v_fma_f32 v25, v8, v53, v25
	s_waitcnt lgkmcnt(2)
	v_fma_f32 v24, v10, v64, v24
	v_fma_f32 v25, v10, v65, v25
	s_waitcnt lgkmcnt(1)
	v_fma_f32 v24, v12, v68, v24
	v_fma_f32 v25, v12, v69, v25
	s_waitcnt lgkmcnt(0)
	v_fma_f32 v68, v14, v72, v24
	v_fma_f32 v69, v14, v73, v25
	v_mul_f32_e32 v24, v4, v30
	v_mul_f32_e32 v25, v4, v31
	v_fma_f32 v24, v6, v46, v24
	v_fma_f32 v25, v6, v47, v25
	v_fma_f32 v24, v8, v54, v24
	v_fma_f32 v25, v8, v55, v25
	v_fma_f32 v24, v10, v66, v24
	v_fma_f32 v25, v10, v67, v25
	v_fma_f32 v28, v12, v70, v24
	v_fma_f32 v29, v12, v71, v25
	ds_read_b128 v[24:27], v5 offset:3840
	v_fma_f32 v70, v14, v74, v28
	v_fma_f32 v71, v14, v75, v29
	ds_read_b128 v[28:31], v5 offset:7648
	ds_read_b128 v[32:35], v5 offset:3856
	ds_read_b128 v[40:43], v5 offset:11456
	ds_read_b128 v[44:47], v5 offset:7664
	v_mul_f32_e32 v36, v4, v36
	v_mul_f32_e32 v37, v4, v37
	s_waitcnt lgkmcnt(4)
	v_fma_f32 v24, v6, v24, v36
	v_fma_f32 v25, v6, v25, v37
	ds_read_b128 v[48:51], v5 offset:15264
	ds_read_b128 v[52:55], v5 offset:19072
	ds_read_b128 v[56:59], v5 offset:11472
	s_waitcnt lgkmcnt(6)
	v_fma_f32 v24, v8, v28, v24
	v_fma_f32 v25, v8, v29, v25
	s_waitcnt lgkmcnt(4)
	v_fma_f32 v24, v10, v40, v24
	v_fma_f32 v25, v10, v41, v25
	s_waitcnt lgkmcnt(2)
	v_fma_f32 v24, v12, v48, v24
	v_fma_f32 v25, v12, v49, v25
	s_waitcnt lgkmcnt(1)
	v_fma_f32 v36, v14, v52, v24
	v_fma_f32 v37, v14, v53, v25
	v_mul_f32_e32 v24, v4, v38
	v_mul_f32_e32 v25, v4, v39
	v_fma_f32 v24, v6, v26, v24
	v_fma_f32 v25, v6, v27, v25
	v_fma_f32 v28, v8, v30, v24
	v_fma_f32 v29, v8, v31, v25
	ds_read_b128 v[24:27], v5 offset:22848
	v_fma_f32 v38, v10, v42, v28
	v_fma_f32 v39, v10, v43, v29
	ds_read_b128 v[28:31], v5 offset:22864
	ds_read_b128 v[60:63], v5 offset:15280
	ds_read_b128 v[64:67], v5 offset:19088
	v_mul_f32_e32 v16, v15, v13
	v_mul_f32_e32 v0, v4, v0
	v_mul_f32_e32 v1, v4, v1
	s_waitcnt lgkmcnt(3)
	v_fma_f32 v40, v16, v24, v76
	v_fma_f32 v41, v16, v25, v77
	v_fma_f32 v78, v16, v26, v78
	v_fma_f32 v79, v16, v27, v79
	s_waitcnt lgkmcnt(2)
	v_fma_f32 v80, v16, v28, v68
	v_fma_f32 v81, v16, v29, v69
	v_fma_f32 v82, v16, v30, v70
	v_fma_f32 v83, v16, v31, v71
	v_fma_f32 v0, v6, v32, v0
	v_fma_f32 v1, v6, v33, v1
	ds_read_b128 v[24:27], v5 offset:22880
	ds_read_b128 v[28:31], v5 offset:22896
	v_fma_f32 v0, v8, v44, v0
	v_fma_f32 v1, v8, v45, v1
	v_fma_f32 v0, v10, v56, v0
	v_fma_f32 v1, v10, v57, v1
	s_waitcnt lgkmcnt(3)
	v_fma_f32 v0, v12, v60, v0
	v_fma_f32 v1, v12, v61, v1
	s_waitcnt lgkmcnt(2)
	v_fma_f32 v0, v14, v64, v0
	v_fma_f32 v1, v14, v65, v1
	s_waitcnt lgkmcnt(0)
	v_fma_f32 v88, v16, v28, v0
	v_fma_f32 v89, v16, v29, v1
	v_mul_f32_e32 v0, v4, v2
	v_mul_f32_e32 v1, v4, v3
	v_fma_f32 v0, v6, v34, v0
	v_fma_f32 v1, v6, v35, v1
	v_fma_f32 v0, v8, v46, v0
	v_fma_f32 v1, v8, v47, v1
	v_fma_f32 v0, v10, v58, v0
	v_fma_f32 v1, v10, v59, v1
	v_fma_f32 v38, v12, v50, v38
	v_fma_f32 v39, v12, v51, v39
	v_fma_f32 v84, v16, v24, v36
	v_fma_f32 v85, v16, v25, v37
	v_fma_f32 v24, v12, v62, v0
	v_fma_f32 v25, v12, v63, v1
	ds_read_b128 v[0:3], v5 offset:64
	v_fma_f32 v38, v14, v54, v38
	v_fma_f32 v39, v14, v55, v39
	v_fma_f32 v24, v14, v66, v24
	v_fma_f32 v25, v14, v67, v25
	v_fma_f32 v86, v16, v26, v38
	v_fma_f32 v87, v16, v27, v39
	v_fma_f32 v90, v16, v30, v24
	v_fma_f32 v91, v16, v31, v25
	ds_read_b128 v[24:27], v5 offset:3872
	ds_read_b128 v[36:39], v5 offset:80
	ds_read_b128 v[28:31], v5 offset:7680
	ds_read_b128 v[42:45], v5 offset:3888
	ds_read_b128 v[32:35], v5 offset:11488
	ds_read_b128 v[46:49], v5 offset:7696
	s_waitcnt lgkmcnt(6)
	v_mul_f32_e32 v0, v4, v0
	v_mul_f32_e32 v1, v4, v1
	ds_read_b128 v[50:53], v5 offset:15296
	ds_read_b128 v[54:57], v5 offset:11504
	s_waitcnt lgkmcnt(7)
	v_fma_f32 v0, v6, v24, v0
	v_fma_f32 v1, v6, v25, v1
	s_waitcnt lgkmcnt(5)
	v_fma_f32 v0, v8, v28, v0
	v_fma_f32 v1, v8, v29, v1
	ds_read_b128 v[58:61], v5 offset:19104
	ds_read_b128 v[62:65], v5 offset:22912
	ds_read_b128 v[66:69], v5 offset:15312
	s_waitcnt lgkmcnt(6)
	v_fma_f32 v0, v10, v32, v0
	v_fma_f32 v1, v10, v33, v1
	s_waitcnt lgkmcnt(4)
	v_fma_f32 v0, v12, v50, v0
	v_fma_f32 v1, v12, v51, v1
	s_waitcnt lgkmcnt(2)
	v_fma_f32 v0, v14, v58, v0
	v_fma_f32 v1, v14, v59, v1
	s_waitcnt lgkmcnt(1)
	v_fma_f32 v62, v16, v62, v0
	v_fma_f32 v63, v16, v63, v1
	v_mul_f32_e32 v0, v4, v2
	v_mul_f32_e32 v1, v4, v3
	v_fma_f32 v0, v6, v26, v0
	v_fma_f32 v1, v6, v27, v1
	v_fma_f32 v0, v8, v30, v0
	v_fma_f32 v1, v8, v31, v1
	ds_read_b128 v[74:77], v5 offset:22928
	v_fma_f32 v24, v10, v34, v0
	v_fma_f32 v25, v10, v35, v1
	ds_read_b128 v[0:3], v5 offset:26656
	ds_read_b128 v[28:31], v5 offset:26672
	ds_read_b128 v[32:35], v5 offset:26688
	v_fma_f32 v24, v12, v52, v24
	v_fma_f32 v25, v12, v53, v25
	v_mul_f32_e32 v18, v15, v7
	ds_read_b128 v[70:73], v5 offset:19120
	v_fma_f32 v24, v14, v60, v24
	v_fma_f32 v25, v14, v61, v25
	v_mul_f32_e32 v36, v4, v36
	v_mul_f32_e32 v37, v4, v37
	v_mul_f32_e32 v38, v4, v38
	v_mul_f32_e32 v39, v4, v39
	v_fma_f32 v64, v16, v64, v24
	v_fma_f32 v65, v16, v65, v25
	s_waitcnt lgkmcnt(3)
	v_fma_f32 v24, v18, v0, v40
	v_fma_f32 v25, v18, v1, v41
	v_fma_f32 v26, v18, v2, v78
	v_fma_f32 v27, v18, v3, v79
	s_waitcnt lgkmcnt(2)
	v_fma_f32 v0, v18, v28, v80
	v_fma_f32 v1, v18, v29, v81
	v_fma_f32 v2, v18, v30, v82
	v_fma_f32 v3, v18, v31, v83
	ds_read_b128 v[28:31], v5 offset:26704
	ds_read_b128 v[50:53], v5 offset:26720
	v_fma_f32 v36, v6, v42, v36
	v_fma_f32 v37, v6, v43, v37
	v_fma_f32 v38, v6, v44, v38
	v_fma_f32 v39, v6, v45, v39
	v_fma_f32 v36, v8, v46, v36
	v_fma_f32 v37, v8, v47, v37
	ds_read_b128 v[58:61], v5 offset:26736
	v_fma_f32 v38, v8, v48, v38
	v_fma_f32 v39, v8, v49, v39
	v_fma_f32 v36, v10, v54, v36
	v_fma_f32 v37, v10, v55, v37
	v_fma_f32 v38, v10, v56, v38
	v_fma_f32 v39, v10, v57, v39
	v_fma_f32 v36, v12, v66, v36
	v_fma_f32 v37, v12, v67, v37
	v_fma_f32 v38, v12, v68, v38
	v_fma_f32 v39, v12, v69, v39
	ds_read_b128 v[44:47], v5 offset:96
	s_waitcnt lgkmcnt(4)
	v_fma_f32 v36, v14, v70, v36
	v_fma_f32 v37, v14, v71, v37
	v_fma_f32 v38, v14, v72, v38
	v_fma_f32 v39, v14, v73, v39
	v_fma_f32 v36, v16, v74, v36
	v_fma_f32 v37, v16, v75, v37
	s_waitcnt lgkmcnt(3)
	v_fma_f32 v40, v18, v28, v88
	v_fma_f32 v41, v18, v29, v89
	v_fma_f32 v42, v18, v30, v90
	v_fma_f32 v43, v18, v31, v91
	s_waitcnt lgkmcnt(2)
	v_fma_f32 v30, v18, v50, v62
	v_fma_f32 v31, v18, v51, v63
	v_fma_f32 v28, v18, v52, v64
	v_fma_f32 v29, v18, v53, v65
	v_fma_f32 v38, v16, v76, v38
	v_fma_f32 v39, v16, v77, v39
	ds_read_b128 v[48:51], v5 offset:3904
	ds_read_b128 v[52:55], v5 offset:112
	v_fma_f32 v32, v18, v32, v84
	v_fma_f32 v33, v18, v33, v85
	v_fma_f32 v34, v18, v34, v86
	v_fma_f32 v35, v18, v35, v87
	s_waitcnt lgkmcnt(3)
	v_fma_f32 v36, v18, v58, v36
	v_fma_f32 v37, v18, v59, v37
	v_fma_f32 v38, v18, v60, v38
	v_fma_f32 v39, v18, v61, v39
	ds_read_b128 v[56:59], v5 offset:7712
	ds_read_b128 v[60:63], v5 offset:3920
	ds_read_b128 v[64:67], v5 offset:11520
	ds_read_b128 v[68:71], v5 offset:7728
	ds_read_b128 v[72:75], v5 offset:15328
	ds_read_b128 v[76:79], v5 offset:11536
	ds_read_b128 v[80:83], v5 offset:19136
	ds_read_b128 v[84:87], v5 offset:15344
	ds_read_b128 v[88:91], v5 offset:22944
	ds_read_b128 v[92:95], v5 offset:19152
	ds_read_b128 v[96:99], v5 offset:26752
	ds_read_b128 v[100:103], v5 offset:30464
	ds_read_b128 v[104:107], v5 offset:22960
	s_waitcnt lgkmcnt(14)
	v_mul_f32_e32 v44, v4, v44
	v_mul_f32_e32 v45, v4, v45
	v_fma_f32 v44, v6, v48, v44
	v_fma_f32 v45, v6, v49, v45
	ds_read_b128 v[116:119], v5 offset:30496
	s_waitcnt lgkmcnt(13)
	v_fma_f32 v44, v8, v56, v44
	v_fma_f32 v45, v8, v57, v45
	s_waitcnt lgkmcnt(2)
	v_fma_f32 v48, v20, v100, v24
	v_fma_f32 v49, v20, v101, v25
	v_fma_f32 v56, v20, v102, v26
	v_fma_f32 v57, v20, v103, v27
	ds_read_b128 v[24:27], v5 offset:30512
	s_waitcnt lgkmcnt(1)
	v_fma_f32 v32, v20, v116, v32
	v_fma_f32 v33, v20, v117, v33
	v_fma_f32 v34, v20, v118, v34
	v_fma_f32 v35, v20, v119, v35
	ds_read_b128 v[108:111], v5 offset:26768
	ds_read_b128 v[112:115], v5 offset:30480
	s_waitcnt lgkmcnt(2)
	v_fma_f32 v40, v20, v24, v40
	v_fma_f32 v41, v20, v25, v41
	v_cvt_pk_f16_f32 v24, v32, v33
	v_mul_f32_e32 v32, v4, v46
	v_mul_f32_e32 v33, v4, v47
	v_fma_f32 v32, v6, v50, v32
	v_fma_f32 v33, v6, v51, v33
	v_fma_f32 v32, v8, v58, v32
	v_fma_f32 v33, v8, v59, v33
	v_fma_f32 v32, v10, v66, v32
	v_fma_f32 v33, v10, v67, v33
	v_fma_f32 v42, v20, v26, v42
	v_fma_f32 v43, v20, v27, v43
	v_cvt_pk_f16_f32 v25, v34, v35
	v_cvt_pk_f16_f32 v26, v40, v41
	v_fma_f32 v40, v12, v74, v32
	v_fma_f32 v41, v12, v75, v33
	ds_read_b128 v[32:35], v5 offset:30528
	v_fma_f32 v40, v14, v82, v40
	v_fma_f32 v41, v14, v83, v41
	v_cvt_pk_f16_f32 v27, v42, v43
	v_fma_f32 v46, v16, v90, v40
	v_fma_f32 v47, v16, v91, v41
	ds_read_b128 v[40:43], v5 offset:30544
	v_fma_f32 v44, v10, v64, v44
	v_fma_f32 v45, v10, v65, v45
	s_waitcnt lgkmcnt(2)
	v_fma_f32 v64, v20, v112, v0
	v_fma_f32 v65, v20, v113, v1
	v_cvt_pk_f16_f32 v0, v48, v49
	s_waitcnt lgkmcnt(1)
	v_fma_f32 v48, v20, v32, v30
	v_fma_f32 v49, v20, v33, v31
	ds_read_b128 v[30:33], v5 offset:30560
	v_fma_f32 v44, v12, v72, v44
	v_fma_f32 v45, v12, v73, v45
	v_fma_f32 v44, v14, v80, v44
	v_fma_f32 v45, v14, v81, v45
	v_fma_f32 v44, v16, v88, v44
	v_fma_f32 v45, v16, v89, v45
	v_fma_f32 v72, v20, v114, v2
	v_fma_f32 v73, v20, v115, v3
	v_fma_f32 v44, v18, v96, v44
	v_fma_f32 v45, v18, v97, v45
	v_cvt_pk_f16_f32 v1, v56, v57
	v_cvt_pk_f16_f32 v2, v64, v65
	v_cvt_pk_f16_f32 v3, v72, v73
	v_fma_f32 v50, v20, v34, v28
	v_fma_f32 v51, v20, v35, v29
	s_waitcnt lgkmcnt(1)
	v_fma_f32 v40, v20, v40, v36
	v_fma_f32 v41, v20, v41, v37
	v_fma_f32 v38, v20, v42, v38
	v_fma_f32 v39, v20, v43, v39
	ds_read_b128 v[34:37], v5 offset:30576
	s_waitcnt lgkmcnt(1)
	v_fma_f32 v42, v20, v30, v44
	v_fma_f32 v43, v20, v31, v45
	v_cvt_pk_f16_f32 v28, v48, v49
	v_cvt_pk_f16_f32 v29, v50, v51
	v_cvt_pk_f16_f32 v30, v40, v41
	v_cvt_pk_f16_f32 v31, v38, v39
	v_mul_f32_e32 v38, v4, v52
	v_mul_f32_e32 v39, v4, v53
	global_store_dwordx4 v[22:23], v[0:3], off
	global_store_dwordx4 v[22:23], v[24:27], off offset:16
	global_store_dwordx4 v[22:23], v[28:31], off offset:32
	v_mul_f32_e32 v0, v4, v54
	v_mul_f32_e32 v1, v4, v55
	v_fma_f32 v38, v6, v60, v38
	v_fma_f32 v39, v6, v61, v39
	v_fma_f32 v0, v6, v62, v0
	v_fma_f32 v1, v6, v63, v1
	v_fma_f32 v38, v8, v68, v38
	v_fma_f32 v39, v8, v69, v39
	v_fma_f32 v0, v8, v70, v0
	v_fma_f32 v1, v8, v71, v1
	v_fma_f32 v38, v10, v76, v38
	v_fma_f32 v39, v10, v77, v39
	v_fma_f32 v0, v10, v78, v0
	v_fma_f32 v1, v10, v79, v1
	v_fma_f32 v38, v12, v84, v38
	v_fma_f32 v39, v12, v85, v39
	v_fma_f32 v0, v12, v86, v0
	v_fma_f32 v1, v12, v87, v1
	v_fma_f32 v38, v14, v92, v38
	v_fma_f32 v39, v14, v93, v39
	v_fma_f32 v0, v14, v94, v0
	v_fma_f32 v1, v14, v95, v1
	v_fma_f32 v38, v16, v104, v38
	v_fma_f32 v39, v16, v105, v39
	v_fma_f32 v0, v16, v106, v0
	v_fma_f32 v1, v16, v107, v1
	v_fma_f32 v46, v18, v98, v46
	v_fma_f32 v47, v18, v99, v47
	v_fma_f32 v38, v18, v108, v38
	v_fma_f32 v39, v18, v109, v39
	v_fma_f32 v0, v18, v110, v0
	v_fma_f32 v1, v18, v111, v1
	v_fma_f32 v44, v20, v32, v46
	v_fma_f32 v45, v20, v33, v47
	s_waitcnt lgkmcnt(0)
	v_fma_f32 v34, v20, v34, v38
	v_fma_f32 v35, v20, v35, v39
	v_fma_f32 v0, v20, v36, v0
	v_fma_f32 v1, v20, v37, v1
	v_cvt_pk_f16_f32 v32, v42, v43
	v_cvt_pk_f16_f32 v33, v44, v45
	v_cvt_pk_f16_f32 v34, v34, v35
	v_cvt_pk_f16_f32 v35, v0, v1
	global_store_dwordx4 v[22:23], v[32:35], off offset:48
